# wq GEMM epilogue: all eight rstd quarter loads issued up front instead of one load + vmcnt(0) per row group behind the previous stores
# speedup vs baseline: 1.0326x; 1.0010x over previous
; __device__ __forceinline__ u32x4 pack8(const f32x4 a, const f32x4 b) { u32x4 w; w.x = cvt_pk_bf16(a[0], a[1]); w.y = cvt_pk_bf16(a[2], a[3]); w.z = cvt_pk_bf16(b[0], b[1]); w.w = cvt_pk_bf16(b[2], b[3]); return w; }
; __device__ __forceinline__ float rstd_of4(const float* ss, int row, int fq) { const f32x4 a = *(const f32x4*)(ss + (size_t)row * 16 + fq * 4); float s = (a[0] + a[1]) + (a[2] + a[3]);
;     s += __shfl_xor(s, 16); s += __shfl_xor(s, 32); return __builtin_amdgcn_rsqf(s * (1.f / 1024.f) + 1e-6f); }
;     __device__ __forceinline__ void operator()(const f32x4 (&acc)[2][2][4][2], const Unit& u, int wr, int wc, int fr, int fq) const {
;         asm volatile("" : "+v"(fr), "+v"(fq));
;         const int row0 = u.pm * BM + wr * 64 + fr, col0 = u.pn * BM + wc * 32 + fq * 8;
; #pragma unroll
;         for (int ai = 0; ai < 2; ++ai)
; #pragma unroll
;             for (int m = 0; m < 4; ++m) { const int row = row0 + ai * HALF + m * 16; const float rs = rstd_of4(ss, row, fq) * scale;
; #pragma unroll
;                 for (int bj = 0; bj < 2; ++bj) *(u32x4*)(O + (size_t)row * ldc + col0 + bj * HALF) = pack8(acc[ai][bj][m][0] * rs, acc[ai][bj][m][1] * rs); asm volatile("" ::: "memory"); }
;     }
.LBB0_1501:
	s_lshl_b32 s4, s66, 8
	v_mov_b32_e32 v5, v182
	v_mov_b32_e32 v4, v1
	s_add_i32 s4, s4, s22
	v_and_b32_e32 v7, 64, v246
	v_add_u32_e32 v6, s4, v4
	s_lshl_b32 s4, s65, 8
	s_or_b32 s4, s4, s23
	v_lshl_add_u32 v4, v5, 3, s4
	v_lshlrev_b32_e32 v8, 2, v5
	v_xor_b32_e32 v5, 16, v246
	v_add_u32_e32 v7, 64, v7
	v_cmp_lt_i32_e32 vcc, v5, v7
	v_ashrrev_i32_e32 v9, 31, v8
	v_lshlrev_b64 v[8:9], 2, v[8:9]
	v_cndmask_b32_e32 v5, v246, v5, vcc
	v_lshlrev_b32_e32 v10, 2, v5
	v_xor_b32_e32 v5, 32, v246
	v_cmp_lt_i32_e32 vcc, v5, v7
	v_ashrrev_i32_e32 v7, 31, v6
	v_lshlrev_b64 v[12:13], 6, v[6:7]
	v_lshl_add_u64 v[12:13], s[44:45], 0, v[12:13]
	v_lshl_add_u64 v[12:13], v[12:13], 0, v[8:9]
	global_load_dwordx4 v[12:15], v[12:13], off
	v_add_u32_e32 v24, 16, v6
	v_ashrrev_i32_e32 v25, 31, v24
	v_lshlrev_b64 v[24:25], 6, v[24:25]
	v_lshl_add_u64 v[24:25], s[44:45], 0, v[24:25]
	v_lshl_add_u64 v[24:25], v[24:25], 0, v[8:9]
	global_load_dwordx4 v[24:27], v[24:25], off
	v_add_u32_e32 v28, 32, v6
	v_ashrrev_i32_e32 v29, 31, v28
	v_lshlrev_b64 v[28:29], 6, v[28:29]
	v_lshl_add_u64 v[28:29], s[44:45], 0, v[28:29]
	v_lshl_add_u64 v[28:29], v[28:29], 0, v[8:9]
	global_load_dwordx4 v[28:31], v[28:29], off
	v_add_u32_e32 v32, 48, v6
	v_ashrrev_i32_e32 v33, 31, v32
	v_lshlrev_b64 v[32:33], 6, v[32:33]
	v_lshl_add_u64 v[32:33], s[44:45], 0, v[32:33]
	v_lshl_add_u64 v[32:33], v[32:33], 0, v[8:9]
	global_load_dwordx4 v[32:35], v[32:33], off
	v_add_u32_e32 v208, 0x80, v6
	v_ashrrev_i32_e32 v209, 31, v208
	v_lshlrev_b64 v[208:209], 6, v[208:209]
	v_lshl_add_u64 v[208:209], s[44:45], 0, v[208:209]
	v_lshl_add_u64 v[208:209], v[208:209], 0, v[8:9]
	global_load_dwordx4 v[208:211], v[208:209], off
	v_add_u32_e32 v212, 0x90, v6
	v_ashrrev_i32_e32 v213, 31, v212
	v_lshlrev_b64 v[212:213], 6, v[212:213]
	v_lshl_add_u64 v[212:213], s[44:45], 0, v[212:213]
	v_lshl_add_u64 v[212:213], v[212:213], 0, v[8:9]
	global_load_dwordx4 v[212:215], v[212:213], off
	v_add_u32_e32 v216, 0xa0, v6
	v_ashrrev_i32_e32 v217, 31, v216
	v_lshlrev_b64 v[216:217], 6, v[216:217]
	v_lshl_add_u64 v[216:217], s[44:45], 0, v[216:217]
	v_lshl_add_u64 v[216:217], v[216:217], 0, v[8:9]
	global_load_dwordx4 v[216:219], v[216:217], off
	v_add_u32_e32 v220, 0xb0, v6
	v_ashrrev_i32_e32 v221, 31, v220
	v_lshlrev_b64 v[220:221], 6, v[220:221]
	v_lshl_add_u64 v[220:221], s[44:45], 0, v[220:221]
	v_lshl_add_u64 v[220:221], v[220:221], 0, v[8:9]
	global_load_dwordx4 v[220:223], v[220:221], off
	v_cndmask_b32_e32 v5, v246, v5, vcc
	v_lshlrev_b32_e32 v11, 2, v5
	v_ashrrev_i32_e32 v5, 31, v4
	v_lshlrev_b64 v[4:5], 1, v[4:5]
	s_mov_b64 s[4:5], -1
	s_andn2_b64 vcc, exec, s[40:41]
	s_waitcnt vmcnt(0)
	v_mov_b32_e32 v16, v13
	v_mov_b32_e32 v17, v14
	v_mov_b32_e32 v13, v15
	v_pk_add_f32 v[12:13], v[16:17], v[12:13]
	s_nop 0
	v_add_f32_e32 v12, v12, v13
	ds_bpermute_b32 v13, v10, v12
	s_waitcnt lgkmcnt(0)
	v_add_f32_e32 v12, v12, v13
	ds_bpermute_b32 v13, v11, v12
	s_waitcnt lgkmcnt(0)
	v_add_f32_e32 v12, v12, v13
	v_fmamk_f32 v12, v12, 0x3a800000, v227
	v_rsq_f32_e32 v12, v12
	s_nop 0
	v_mul_f32_e32 v16, 0x3ab8aa3b, v12
	v_pk_mul_f32 v[14:15], v[162:163], v[16:17] op_sel_hi:[1,0]
	v_pk_mul_f32 v[12:13], v[160:161], v[16:17] op_sel_hi:[1,0]
	v_pk_mul_f32 v[18:19], v[158:159], v[16:17] op_sel_hi:[1,0]
	v_pk_mul_f32 v[20:21], v[156:157], v[16:17] op_sel_hi:[1,0]
	v_cvt_pk_bf16_f32 v12, v12, v13
	v_cvt_pk_bf16_f32 v13, v14, v15
	s_nop 0
	v_cvt_pk_bf16_f32 v14, v20, v21
	v_cvt_pk_bf16_f32 v15, v18, v19
	v_lshlrev_b64 v[18:19], 11, v[6:7]
	v_lshl_add_u64 v[18:19], s[42:43], 0, v[18:19]
	v_lshl_add_u64 v[18:19], v[18:19], 0, v[4:5]
	global_store_dwordx4 v[18:19], v[12:15], off
	v_pk_mul_f32 v[20:21], v[150:151], v[16:17] op_sel_hi:[1,0]
	s_nop 0
	v_pk_mul_f32 v[14:15], v[154:155], v[16:17] op_sel_hi:[1,0]
	v_pk_mul_f32 v[12:13], v[152:153], v[16:17] op_sel_hi:[1,0]
	v_pk_mul_f32 v[16:17], v[148:149], v[16:17] op_sel_hi:[1,0]
	v_cvt_pk_bf16_f32 v12, v12, v13
	v_cvt_pk_bf16_f32 v13, v14, v15
	s_nop 0
	v_cvt_pk_bf16_f32 v14, v16, v17
	v_add_u32_e32 v16, 16, v6
	v_ashrrev_i32_e32 v17, 31, v16
	v_cvt_pk_bf16_f32 v15, v20, v21
	global_store_dwordx4 v[18:19], v[12:15], off offset:256
	s_nop 1
	v_lshlrev_b64 v[12:13], 6, v[16:17]
	v_lshl_add_u64 v[12:13], s[44:45], 0, v[12:13]
	v_lshl_add_u64 v[12:13], v[12:13], 0, v[8:9]
	v_mov_b64_e32 v[12:13], v[24:25]
	v_mov_b64_e32 v[14:15], v[26:27]
	v_lshlrev_b64 v[16:17], 11, v[16:17]
	v_lshl_add_u64 v[16:17], s[42:43], 0, v[16:17]
	v_lshl_add_u64 v[16:17], v[16:17], 0, v[4:5]
	v_mov_b32_e32 v18, v13
	v_mov_b32_e32 v19, v14
	v_mov_b32_e32 v13, v15
	v_pk_add_f32 v[12:13], v[18:19], v[12:13]
	s_nop 0
	v_add_f32_e32 v7, v12, v13
	ds_bpermute_b32 v12, v10, v7
	s_waitcnt lgkmcnt(0)
	v_add_f32_e32 v7, v7, v12
	ds_bpermute_b32 v12, v11, v7
	s_waitcnt lgkmcnt(0)
	v_add_f32_e32 v7, v7, v12
	v_fmamk_f32 v7, v7, 0x3a800000, v227
	v_rsq_f32_e32 v7, v7
	s_nop 0
	v_mul_f32_e32 v18, 0x3ab8aa3b, v7
	v_pk_mul_f32 v[14:15], v[146:147], v[18:19] op_sel_hi:[1,0]
	v_pk_mul_f32 v[12:13], v[144:145], v[18:19] op_sel_hi:[1,0]
	v_pk_mul_f32 v[20:21], v[142:143], v[18:19] op_sel_hi:[1,0]
	v_pk_mul_f32 v[22:23], v[140:141], v[18:19] op_sel_hi:[1,0]
	v_cvt_pk_bf16_f32 v12, v12, v13
	v_cvt_pk_bf16_f32 v13, v14, v15
	s_nop 0
	v_cvt_pk_bf16_f32 v14, v22, v23
	v_cvt_pk_bf16_f32 v15, v20, v21
	global_store_dwordx4 v[16:17], v[12:15], off
	v_pk_mul_f32 v[20:21], v[134:135], v[18:19] op_sel_hi:[1,0]
	s_nop 0
	v_pk_mul_f32 v[14:15], v[138:139], v[18:19] op_sel_hi:[1,0]
	v_pk_mul_f32 v[12:13], v[136:137], v[18:19] op_sel_hi:[1,0]
	v_pk_mul_f32 v[18:19], v[132:133], v[18:19] op_sel_hi:[1,0]
	v_cvt_pk_bf16_f32 v12, v12, v13
	v_cvt_pk_bf16_f32 v13, v14, v15
	s_nop 0
	v_cvt_pk_bf16_f32 v14, v18, v19
	v_cvt_pk_bf16_f32 v15, v20, v21
	global_store_dwordx4 v[16:17], v[12:15], off offset:256
	v_add_u32_e32 v16, 32, v6
	v_ashrrev_i32_e32 v17, 31, v16
	v_lshlrev_b64 v[12:13], 6, v[16:17]
	v_lshl_add_u64 v[12:13], s[44:45], 0, v[12:13]
	v_lshl_add_u64 v[12:13], v[12:13], 0, v[8:9]
	v_mov_b64_e32 v[12:13], v[28:29]
	v_mov_b64_e32 v[14:15], v[30:31]
	v_lshlrev_b64 v[16:17], 11, v[16:17]
	v_lshl_add_u64 v[16:17], s[42:43], 0, v[16:17]
	v_lshl_add_u64 v[16:17], v[16:17], 0, v[4:5]
	v_mov_b32_e32 v18, v13
	v_mov_b32_e32 v19, v14
	v_mov_b32_e32 v13, v15
	v_pk_add_f32 v[12:13], v[18:19], v[12:13]
	s_nop 0
	v_add_f32_e32 v7, v12, v13
	ds_bpermute_b32 v12, v10, v7
	s_waitcnt lgkmcnt(0)
; __device__ __forceinline__ u32x4 pack8(const f32x4 a, const f32x4 b) { u32x4 w; w.x = cvt_pk_bf16(a[0], a[1]); w.y = cvt_pk_bf16(a[2], a[3]); w.z = cvt_pk_bf16(b[0], b[1]); w.w = cvt_pk_bf16(b[2], b[3]); return w; }
;     __device__ __forceinline__ void operator()(const f32x4 (&acc)[2][2][4][2], const Unit& u, int wr, int wc, int fr, int fq) const {
;     ...
;             for (int m = 0; m < 4; ++m) { const int row = row0 + ai * HALF + m * 16; const float rs = rstd_of4(ss, row, fq) * scale;
; #pragma unroll
;                 for (int bj = 0; bj < 2; ++bj) *(u32x4*)(O + (size_t)row * ldc + col0 + bj * HALF) = pack8(acc[ai][bj][m][0] * rs, acc[ai][bj][m][1] * rs); asm volatile("" ::: "memory"); }
	v_add_f32_e32 v7, v7, v12
	ds_bpermute_b32 v12, v11, v7
	s_waitcnt lgkmcnt(0)
	v_add_f32_e32 v7, v7, v12
	v_fmamk_f32 v7, v7, 0x3a800000, v227
	v_rsq_f32_e32 v7, v7
	s_nop 0
	v_mul_f32_e32 v18, 0x3ab8aa3b, v7
	v_pk_mul_f32 v[14:15], v[130:131], v[18:19] op_sel_hi:[1,0]
	v_pk_mul_f32 v[12:13], v[128:129], v[18:19] op_sel_hi:[1,0]
	v_pk_mul_f32 v[20:21], v[126:127], v[18:19] op_sel_hi:[1,0]
	v_pk_mul_f32 v[22:23], v[124:125], v[18:19] op_sel_hi:[1,0]
	v_cvt_pk_bf16_f32 v12, v12, v13
	v_cvt_pk_bf16_f32 v13, v14, v15
	s_nop 0
	v_cvt_pk_bf16_f32 v14, v22, v23
	v_cvt_pk_bf16_f32 v15, v20, v21
	global_store_dwordx4 v[16:17], v[12:15], off
	v_pk_mul_f32 v[20:21], v[118:119], v[18:19] op_sel_hi:[1,0]
	s_nop 0
	v_pk_mul_f32 v[14:15], v[122:123], v[18:19] op_sel_hi:[1,0]
	v_pk_mul_f32 v[12:13], v[120:121], v[18:19] op_sel_hi:[1,0]
	v_pk_mul_f32 v[18:19], v[116:117], v[18:19] op_sel_hi:[1,0]
	v_cvt_pk_bf16_f32 v12, v12, v13
	v_cvt_pk_bf16_f32 v13, v14, v15
	s_nop 0
	v_cvt_pk_bf16_f32 v14, v18, v19
	v_cvt_pk_bf16_f32 v15, v20, v21
	global_store_dwordx4 v[16:17], v[12:15], off offset:256
	v_add_u32_e32 v16, 48, v6
	v_ashrrev_i32_e32 v17, 31, v16
	v_lshlrev_b64 v[12:13], 6, v[16:17]
	v_lshl_add_u64 v[12:13], s[44:45], 0, v[12:13]
	v_lshl_add_u64 v[12:13], v[12:13], 0, v[8:9]
	v_mov_b64_e32 v[12:13], v[32:33]
	v_mov_b64_e32 v[14:15], v[34:35]
	v_lshlrev_b64 v[16:17], 11, v[16:17]
	v_lshl_add_u64 v[16:17], s[42:43], 0, v[16:17]
	v_lshl_add_u64 v[16:17], v[16:17], 0, v[4:5]
	v_mov_b32_e32 v18, v13
	v_mov_b32_e32 v19, v14
	v_mov_b32_e32 v13, v15
	v_pk_add_f32 v[12:13], v[18:19], v[12:13]
	s_nop 0
	v_add_f32_e32 v7, v12, v13
	ds_bpermute_b32 v12, v10, v7
	s_waitcnt lgkmcnt(0)
	v_add_f32_e32 v7, v7, v12
	ds_bpermute_b32 v12, v11, v7
	s_waitcnt lgkmcnt(0)
	v_add_f32_e32 v7, v7, v12
	v_fmamk_f32 v7, v7, 0x3a800000, v227
	v_rsq_f32_e32 v7, v7
	s_nop 0
	v_mul_f32_e32 v18, 0x3ab8aa3b, v7
	v_pk_mul_f32 v[14:15], v[114:115], v[18:19] op_sel_hi:[1,0]
	v_pk_mul_f32 v[12:13], v[112:113], v[18:19] op_sel_hi:[1,0]
	v_pk_mul_f32 v[20:21], v[110:111], v[18:19] op_sel_hi:[1,0]
	v_pk_mul_f32 v[22:23], v[108:109], v[18:19] op_sel_hi:[1,0]
	v_cvt_pk_bf16_f32 v12, v12, v13
	v_cvt_pk_bf16_f32 v13, v14, v15
	s_nop 0
	v_cvt_pk_bf16_f32 v14, v22, v23
	v_cvt_pk_bf16_f32 v15, v20, v21
	global_store_dwordx4 v[16:17], v[12:15], off
	v_pk_mul_f32 v[20:21], v[102:103], v[18:19] op_sel_hi:[1,0]
	s_nop 0
	v_pk_mul_f32 v[14:15], v[106:107], v[18:19] op_sel_hi:[1,0]
	v_pk_mul_f32 v[12:13], v[104:105], v[18:19] op_sel_hi:[1,0]
	v_pk_mul_f32 v[18:19], v[100:101], v[18:19] op_sel_hi:[1,0]
	v_cvt_pk_bf16_f32 v12, v12, v13
	v_cvt_pk_bf16_f32 v13, v14, v15
	s_nop 0
	v_cvt_pk_bf16_f32 v14, v18, v19
	v_cvt_pk_bf16_f32 v15, v20, v21
	global_store_dwordx4 v[16:17], v[12:15], off offset:256
	v_add_u32_e32 v16, 0x80, v6
	v_ashrrev_i32_e32 v17, 31, v16
	v_lshlrev_b64 v[12:13], 6, v[16:17]
	v_lshl_add_u64 v[12:13], s[44:45], 0, v[12:13]
	v_lshl_add_u64 v[12:13], v[12:13], 0, v[8:9]
	v_mov_b64_e32 v[12:13], v[208:209]
	v_mov_b64_e32 v[14:15], v[210:211]
	v_lshlrev_b64 v[16:17], 11, v[16:17]
	v_lshl_add_u64 v[16:17], s[42:43], 0, v[16:17]
	v_lshl_add_u64 v[16:17], v[16:17], 0, v[4:5]
	v_mov_b32_e32 v18, v13
	v_mov_b32_e32 v19, v14
	v_mov_b32_e32 v13, v15
	v_pk_add_f32 v[12:13], v[18:19], v[12:13]
	s_nop 0
	v_add_f32_e32 v7, v12, v13
	ds_bpermute_b32 v12, v10, v7
	s_waitcnt lgkmcnt(0)
	v_add_f32_e32 v7, v7, v12
	ds_bpermute_b32 v12, v11, v7
	s_waitcnt lgkmcnt(0)
	v_add_f32_e32 v7, v7, v12
	v_fmamk_f32 v7, v7, 0x3a800000, v227
	v_rsq_f32_e32 v7, v7
	s_nop 0
	v_mul_f32_e32 v18, 0x3ab8aa3b, v7
	v_pk_mul_f32 v[14:15], v[98:99], v[18:19] op_sel_hi:[1,0]
	v_pk_mul_f32 v[12:13], v[96:97], v[18:19] op_sel_hi:[1,0]
	v_pk_mul_f32 v[20:21], v[94:95], v[18:19] op_sel_hi:[1,0]
	v_pk_mul_f32 v[22:23], v[92:93], v[18:19] op_sel_hi:[1,0]
	v_cvt_pk_bf16_f32 v12, v12, v13
	v_cvt_pk_bf16_f32 v13, v14, v15
	s_nop 0
	v_cvt_pk_bf16_f32 v14, v22, v23
	v_cvt_pk_bf16_f32 v15, v20, v21
	global_store_dwordx4 v[16:17], v[12:15], off
	v_pk_mul_f32 v[20:21], v[86:87], v[18:19] op_sel_hi:[1,0]
	s_nop 0
	v_pk_mul_f32 v[14:15], v[90:91], v[18:19] op_sel_hi:[1,0]
	v_pk_mul_f32 v[12:13], v[88:89], v[18:19] op_sel_hi:[1,0]
	v_pk_mul_f32 v[18:19], v[84:85], v[18:19] op_sel_hi:[1,0]
	v_cvt_pk_bf16_f32 v12, v12, v13
	v_cvt_pk_bf16_f32 v13, v14, v15
	s_nop 0
	v_cvt_pk_bf16_f32 v14, v18, v19
	v_cvt_pk_bf16_f32 v15, v20, v21
	global_store_dwordx4 v[16:17], v[12:15], off offset:256
	v_add_u32_e32 v16, 0x90, v6
	v_ashrrev_i32_e32 v17, 31, v16
	v_lshlrev_b64 v[12:13], 6, v[16:17]
	v_lshl_add_u64 v[12:13], s[44:45], 0, v[12:13]
	v_lshl_add_u64 v[12:13], v[12:13], 0, v[8:9]
	v_mov_b64_e32 v[12:13], v[212:213]
	v_mov_b64_e32 v[14:15], v[214:215]
	v_lshlrev_b64 v[16:17], 11, v[16:17]
	v_lshl_add_u64 v[16:17], s[42:43], 0, v[16:17]
	v_lshl_add_u64 v[16:17], v[16:17], 0, v[4:5]
	v_mov_b32_e32 v18, v13
	v_mov_b32_e32 v19, v14
	v_mov_b32_e32 v13, v15
	v_pk_add_f32 v[12:13], v[18:19], v[12:13]
	s_nop 0
	v_add_f32_e32 v7, v12, v13
	ds_bpermute_b32 v12, v10, v7
	s_waitcnt lgkmcnt(0)
; __device__ __forceinline__ u32x4 pack8(const f32x4 a, const f32x4 b) { u32x4 w; w.x = cvt_pk_bf16(a[0], a[1]); w.y = cvt_pk_bf16(a[2], a[3]); w.z = cvt_pk_bf16(b[0], b[1]); w.w = cvt_pk_bf16(b[2], b[3]); return w; }
;     __device__ __forceinline__ void operator()(const f32x4 (&acc)[2][2][4][2], const Unit& u, int wr, int wc, int fr, int fq) const {
;     ...
;             for (int m = 0; m < 4; ++m) { const int row = row0 + ai * HALF + m * 16; const float rs = rstd_of4(ss, row, fq) * scale;
; #pragma unroll
;                 for (int bj = 0; bj < 2; ++bj) *(u32x4*)(O + (size_t)row * ldc + col0 + bj * HALF) = pack8(acc[ai][bj][m][0] * rs, acc[ai][bj][m][1] * rs); asm volatile("" ::: "memory"); }
	v_add_f32_e32 v7, v7, v12
	ds_bpermute_b32 v12, v11, v7
	s_waitcnt lgkmcnt(0)
	v_add_f32_e32 v7, v7, v12
	v_fmamk_f32 v7, v7, 0x3a800000, v227
	v_rsq_f32_e32 v7, v7
	s_nop 0
	v_mul_f32_e32 v18, 0x3ab8aa3b, v7
	v_pk_mul_f32 v[14:15], v[82:83], v[18:19] op_sel_hi:[1,0]
	v_pk_mul_f32 v[12:13], v[80:81], v[18:19] op_sel_hi:[1,0]
	v_pk_mul_f32 v[20:21], v[78:79], v[18:19] op_sel_hi:[1,0]
	v_pk_mul_f32 v[22:23], v[76:77], v[18:19] op_sel_hi:[1,0]
	v_cvt_pk_bf16_f32 v12, v12, v13
	v_cvt_pk_bf16_f32 v13, v14, v15
	s_nop 0
	v_cvt_pk_bf16_f32 v14, v22, v23
	v_cvt_pk_bf16_f32 v15, v20, v21
	global_store_dwordx4 v[16:17], v[12:15], off
	v_pk_mul_f32 v[20:21], v[70:71], v[18:19] op_sel_hi:[1,0]
	s_nop 0
	v_pk_mul_f32 v[14:15], v[74:75], v[18:19] op_sel_hi:[1,0]
	v_pk_mul_f32 v[12:13], v[72:73], v[18:19] op_sel_hi:[1,0]
	v_pk_mul_f32 v[18:19], v[68:69], v[18:19] op_sel_hi:[1,0]
	v_cvt_pk_bf16_f32 v12, v12, v13
	v_cvt_pk_bf16_f32 v13, v14, v15
	s_nop 0
	v_cvt_pk_bf16_f32 v14, v18, v19
	v_cvt_pk_bf16_f32 v15, v20, v21
	global_store_dwordx4 v[16:17], v[12:15], off offset:256
	v_add_u32_e32 v16, 0xa0, v6
	v_ashrrev_i32_e32 v17, 31, v16
	v_lshlrev_b64 v[12:13], 6, v[16:17]
	v_lshl_add_u64 v[12:13], s[44:45], 0, v[12:13]
	v_lshl_add_u64 v[12:13], v[12:13], 0, v[8:9]
	v_mov_b64_e32 v[12:13], v[216:217]
	v_mov_b64_e32 v[14:15], v[218:219]
	v_lshlrev_b64 v[16:17], 11, v[16:17]
	v_lshl_add_u64 v[16:17], s[42:43], 0, v[16:17]
	v_lshl_add_u64 v[16:17], v[16:17], 0, v[4:5]
	v_mov_b32_e32 v18, v13
	v_mov_b32_e32 v19, v14
	v_mov_b32_e32 v13, v15
	v_pk_add_f32 v[12:13], v[18:19], v[12:13]
	s_nop 0
	v_add_f32_e32 v7, v12, v13
	ds_bpermute_b32 v12, v10, v7
	s_waitcnt lgkmcnt(0)
	v_add_f32_e32 v7, v7, v12
	ds_bpermute_b32 v12, v11, v7
	s_waitcnt lgkmcnt(0)
	v_add_f32_e32 v7, v7, v12
	v_fmamk_f32 v7, v7, 0x3a800000, v227
	v_rsq_f32_e32 v7, v7
	s_nop 0
	v_mul_f32_e32 v18, 0x3ab8aa3b, v7
	v_pk_mul_f32 v[12:13], v[64:65], v[18:19] op_sel_hi:[1,0]
	v_pk_mul_f32 v[14:15], v[66:67], v[18:19] op_sel_hi:[1,0]
	v_cvt_pk_bf16_f32 v12, v12, v13
	v_pk_mul_f32 v[20:21], v[62:63], v[18:19] op_sel_hi:[1,0]
	v_cvt_pk_bf16_f32 v13, v14, v15
	v_pk_mul_f32 v[22:23], v[60:61], v[18:19] op_sel_hi:[1,0]
	s_nop 0
	v_cvt_pk_bf16_f32 v14, v22, v23
	v_cvt_pk_bf16_f32 v15, v20, v21
	global_store_dwordx4 v[16:17], v[12:15], off
	v_pk_mul_f32 v[20:21], v[54:55], v[18:19] op_sel_hi:[1,0]
	s_nop 0
	v_pk_mul_f32 v[12:13], v[56:57], v[18:19] op_sel_hi:[1,0]
	v_pk_mul_f32 v[14:15], v[58:59], v[18:19] op_sel_hi:[1,0]
	v_cvt_pk_bf16_f32 v12, v12, v13
	v_pk_mul_f32 v[18:19], v[52:53], v[18:19] op_sel_hi:[1,0]
	v_cvt_pk_bf16_f32 v13, v14, v15
	s_nop 0
	v_cvt_pk_bf16_f32 v14, v18, v19
	v_cvt_pk_bf16_f32 v15, v20, v21
	global_store_dwordx4 v[16:17], v[12:15], off offset:256
	s_nop 1
	v_add_u32_e32 v12, 0xb0, v6
	v_ashrrev_i32_e32 v13, 31, v12
	v_lshlrev_b64 v[6:7], 6, v[12:13]
	v_lshl_add_u64 v[6:7], s[44:45], 0, v[6:7]
	v_lshl_add_u64 v[6:7], v[6:7], 0, v[8:9]
	v_mov_b64_e32 v[6:7], v[220:221]
	v_mov_b64_e32 v[8:9], v[222:223]
	v_lshlrev_b64 v[12:13], 11, v[12:13]
	v_lshl_add_u64 v[12:13], s[42:43], 0, v[12:13]
	v_lshl_add_u64 v[12:13], v[12:13], 0, v[4:5]
	v_mov_b32_e32 v14, v7
	v_mov_b32_e32 v15, v8
	v_mov_b32_e32 v7, v9
	v_pk_add_f32 v[6:7], v[14:15], v[6:7]
	s_nop 0
	v_add_f32_e32 v6, v6, v7
	ds_bpermute_b32 v7, v10, v6
	s_waitcnt lgkmcnt(0)
	v_add_f32_e32 v6, v6, v7
	ds_bpermute_b32 v7, v11, v6
	s_waitcnt lgkmcnt(0)
	v_add_f32_e32 v6, v6, v7
	v_fmamk_f32 v6, v6, 0x3a800000, v227
	v_rsq_f32_e32 v6, v6
	s_nop 0
	v_mul_f32_e32 v10, 0x3ab8aa3b, v6
	v_pk_mul_f32 v[6:7], v[48:49], v[10:11] op_sel_hi:[1,0]
	v_pk_mul_f32 v[8:9], v[50:51], v[10:11] op_sel_hi:[1,0]
	v_cvt_pk_bf16_f32 v6, v6, v7
	v_pk_mul_f32 v[14:15], v[46:47], v[10:11] op_sel_hi:[1,0]
	v_cvt_pk_bf16_f32 v7, v8, v9
	v_pk_mul_f32 v[16:17], v[44:45], v[10:11] op_sel_hi:[1,0]
	v_pk_mul_f32 v[4:5], v[40:41], v[10:11] op_sel_hi:[1,0]
	v_cvt_pk_bf16_f32 v8, v16, v17
	v_cvt_pk_bf16_f32 v9, v14, v15
	global_store_dwordx4 v[12:13], v[6:9], off
	v_cvt_pk_bf16_f32 v4, v4, v5
	s_nop 1
	v_pk_mul_f32 v[6:7], v[42:43], v[10:11] op_sel_hi:[1,0]
	v_pk_mul_f32 v[8:9], v[38:39], v[10:11] op_sel_hi:[1,0]
	v_pk_mul_f32 v[10:11], v[36:37], v[10:11] op_sel_hi:[1,0]
	v_cvt_pk_bf16_f32 v5, v6, v7
	s_nop 0
	v_cvt_pk_bf16_f32 v6, v10, v11
	v_cvt_pk_bf16_f32 v7, v8, v9
	global_store_dwordx4 v[12:13], v[4:7], off offset:256
	s_cbranch_vccnz .LBB0_1490
	s_andn2_b64 vcc, exec, s[38:39]
	s_cbranch_vccnz .LBB0_1489
	s_barrier
	s_branch .LBB0_1489
